# v24 + early-slot P2 copy groups stop at 15*2048 items too (they were redundantly converting the tail items that the 9-unit workgroups also convert)
# baseline (speedup 1.0000x reference)
.LBB0_219:
	s_cmp_lt_i32 s42, s33
	s_cselect_b64 s[14:15], -1, 0
	s_cmp_ge_i32 s42, s33
	s_cselect_b64 s[8:9], -1, 0
	s_add_u32 s40, s50, 0xd200000
	s_addc_u32 s41, s51, 0
	s_and_b64 vcc, exec, s[8:9]
	s_cbranch_vccnz .LBB0_330
	s_lshl_b32 s0, s86, 3
	s_add_i32 s63, s0, s88
	s_cmp_gt_i32 s63, 0x77ff
	s_waitcnt vmcnt(0)
	s_barrier
	s_cbranch_scc1 .LBB0_329
	s_ashr_i32 s0, s63, 9
	s_mulk_i32 s0, 0x300
	s_and_b32 s22, s63, 0x1ff
	s_add_i32 s23, s0, s22
	s_addk_i32 s23, 0x3000
	s_cmpk_gt_i32 s23, 0x25ff
	s_cbranch_scc0 .LBB0_228
	s_cmpk_gt_u32 s23, 0x27ff
	s_cbranch_scc0 .LBB0_229
	s_cmpk_gt_u32 s23, 0x2bff
	s_cbranch_scc0 .LBB0_230
	s_cmpk_gt_u32 s23, 0x2fff
	s_cbranch_scc0 .LBB0_231
	s_add_i32 s24, s23, 0xffffd000
	s_and_b32 s0, s24, 0xffff
	s_mul_i32 s0, s0, 0xaaab
	s_lshr_b32 s20, s0, 25
	s_mul_i32 s0, s20, 0x300
	s_sub_i32 s0, s24, s0
	s_and_b32 s21, s0, 0xffff
	s_cmpk_gt_u32 s21, 0x1ff
	s_cbranch_scc0 .LBB0_232
	s_cmpk_gt_u32 s24, 0xbfff
	s_cbranch_scc0 .LBB0_233
	s_add_i32 s0, 0, 0x27ea8
	v_mov_b32_e32 v2, s0
	ds_read_b64 v[2:3], v2
	s_mov_b64 s[16:17], 0
	s_waitcnt lgkmcnt(0)
	v_readfirstlane_b32 s0, v2
	v_readfirstlane_b32 s1, v3
	s_branch .LBB0_234

.LBB0_258:
	s_waitcnt lgkmcnt(0)
	s_add_i32 s63, s64, s27
	s_cmp_gt_i32 s63, 0x77ff
	s_cselect_b64 s[18:19], -1, 0

.LBB0_260:
	s_add_i32 s64, s63, s27
	s_cmp_lt_i32 s64, 0x7800
	s_cselect_b64 s[18:19], -1, 0
	s_cmp_gt_i32 s64, 0x77ff
	s_cbranch_scc1 .LBB0_289
	s_ashr_i32 s16, s64, 9
	s_mulk_i32 s16, 0x300
	s_and_b32 s67, s64, 0x1ff
	s_add_i32 s68, s16, s67
	s_addk_i32 s68, 0x3000
	s_cmpk_gt_i32 s68, 0x25ff
	s_mov_b64 s[24:25], -1
	s_cbranch_scc0 .LBB0_286
	s_cmpk_gt_u32 s68, 0x27ff
	s_cbranch_scc0 .LBB0_283
	s_cmpk_gt_u32 s68, 0x2bff
	s_cbranch_scc0 .LBB0_280
	s_cmpk_gt_u32 s68, 0x2fff
	s_cbranch_scc0 .LBB0_277
	s_add_i32 s65, s68, 0xffffd000
	s_and_b32 s16, s65, 0xffff
	s_mul_i32 s16, s16, 0xaaab
	s_lshr_b32 s24, s16, 25
	s_mul_i32 s16, s24, 0x300
	s_sub_i32 s16, s65, s16
	s_and_b32 s25, s16, 0xffff
	s_cmpk_gt_u32 s25, 0x1ff
	s_mov_b64 s[22:23], -1
	s_cbranch_scc0 .LBB0_271
	s_cmpk_gt_u32 s65, 0xbfff
	s_mov_b64 s[20:21], -1
	s_cbranch_scc0 .LBB0_268
	v_mov_b32_e32 v58, s54
	ds_read_b64 v[58:59], v58
	s_mov_b64 s[20:21], 0
	s_waitcnt lgkmcnt(0)
	v_readfirstlane_b32 s16, v58
	v_readfirstlane_b32 s17, v59

.LBB0_292:
	s_waitcnt lgkmcnt(0)
	s_andn2_b64 vcc, exec, s[18:19]
	s_mov_b64 s[18:19], -1
	s_cbranch_vccnz .LBB0_259
	s_add_i32 s67, s53, s63
	s_cmp_gt_i32 s67, 0x77ff
	s_cbranch_scc1 .LBB0_326
	s_ashr_i32 s0, s67, 9
	s_mulk_i32 s0, 0x300
	s_and_b32 s24, s67, 0x1ff
	s_add_i32 s25, s0, s24
	s_addk_i32 s25, 0x3000
	s_cmpk_gt_i32 s25, 0x25ff
	s_mov_b64 s[22:23], -1
	s_cbranch_scc0 .LBB0_323
	s_cmpk_gt_u32 s25, 0x27ff
	s_cbranch_scc0 .LBB0_320
	s_cmpk_gt_u32 s25, 0x2bff
	s_cbranch_scc0 .LBB0_317
	s_cmpk_gt_u32 s25, 0x2fff
	s_cbranch_scc0 .LBB0_314
	s_add_i32 s26, s25, 0xffffd000
	s_and_b32 s0, s26, 0xffff
	s_mul_i32 s0, s0, 0xaaab
	s_lshr_b32 s22, s0, 25
	s_mul_i32 s0, s22, 0x300
	s_sub_i32 s0, s26, s0
	s_and_b32 s23, s0, 0xffff
	s_cmpk_gt_u32 s23, 0x1ff
	s_mov_b64 s[20:21], -1
	s_cbranch_scc0 .LBB0_304
	s_cmpk_gt_u32 s26, 0xbfff
	s_mov_b64 s[18:19], -1
	s_cbranch_scc0 .LBB0_301
	v_mov_b32_e32 v2, s54
	ds_read_b64 v[2:3], v2
	s_mov_b64 s[18:19], 0
	s_waitcnt lgkmcnt(0)
	v_readfirstlane_b32 s0, v2
	v_readfirstlane_b32 s1, v3
